# speedup vs baseline: 1.0286x; 1.0017x over previous
.LBB3_33:
	s_or_b64 exec, exec, s[12:13]
	s_load_dwordx2 s[0:1], s[0:1], 0x30
	s_waitcnt vmcnt(0)
	v_add_u32_e32 v2, s22, v12
	v_or_b32_e32 v2, v2, v14
	v_ashrrev_i32_e32 v3, 31, v2
	v_lshl_add_u64 v[174:175], v[2:3], 4, s[20:21]
	v_and_b32_e32 v2, 48, v0
	s_lshl_b32 s37, s29, 8
	v_lshlrev_b32_e32 v187, 13, v1
	s_lshl_b32 s42, s29, 15
	s_add_i32 s42, s42, 0x630100
	v_lshrrev_b32_e32 v186, 1, v187
	v_add3_u32 v186, v186, v170, s42
	v_lshl_or_b32 v2, v1, 8, v2
	v_lshl_or_b32 v184, v1, 5, s37
	v_add_u32_e32 v1, 0x2000, v187
	v_and_b32_e32 v188, 0xe000, v1
	v_add_u32_e32 v1, 0x4000, v187
	s_ashr_i32 s23, s22, 31
	v_and_b32_e32 v189, 0xe000, v1
	v_add_u32_e32 v1, 0x6000, v187
	s_and_b32 s17, s9, 0xffff
	s_lshl_b64 s[2:3], s[22:23], 1
	v_and_b32_e32 v190, 0xe000, v1
	v_add_u32_e32 v1, 0xa000, v187
	v_and_b32_e32 v0, 31, v0
	v_mov_b32_e32 v177, 0
	s_add_u32 s2, s8, s2
	v_and_b32_e32 v191, 0xe000, v1
	v_add_u32_e32 v1, 0xc000, v187
	s_mov_b32 s16, s8
	v_or_b32_e32 v169, s30, v11
	v_lshlrev_b32_e32 v176, 2, v0
	v_lshlrev_b32_e32 v0, 3, v10
	s_addc_u32 s3, s9, s3
	v_mov_b32_e32 v7, v177
	v_mov_b32_e32 v13, v177
	v_and_b32_e32 v192, 0xe000, v1
	v_add_u32_e32 v1, 0xe000, v187
	s_lshl_b32 s8, s28, 3
	s_mov_b32 s19, 0x20000
	s_mov_b32 s18, 0x6b0100
	v_lshl_add_u64 v[178:179], s[10:11], 0, v[176:177]
	v_add_u32_e32 v185, s30, v10
	s_mov_b32 s36, 1
	v_lshl_add_u64 v[180:181], s[2:3], 0, v[6:7]
	v_lshl_add_u64 v[182:183], s[10:11], 0, v[12:13]
	v_cmp_eq_u32_e64 s[2:3], 0, v10
	v_and_b32_e32 v193, 0xe000, v1
	s_add_i32 s37, s37, s8
	v_xor_b32_e32 v194, 0x8000, v187
	s_mov_b64 s[8:9], 0
	s_mov_b32 s38, 0x186a0
	s_mov_b32 s39, 0x40004000
	s_mov_b32 s40, 0xbb8000
	v_add_u32_e32 v195, v15, v0
	v_mov_b32_e32 v196, 1
	v_mov_b32_e32 v0, v177
	v_mov_b32_e32 v1, v177
	v_mov_b32_e32 v2, v177
	v_mov_b32_e32 v3, v177
	v_mov_b32_e32 v4, v177
	v_mov_b32_e32 v5, v177
	v_mov_b32_e32 v6, v177
	s_waitcnt lgkmcnt(0)
	v_mov_b32_e32 v8, v177
	v_mov_b32_e32 v9, v177
	v_mov_b32_e32 v10, v177
	v_mov_b32_e32 v11, v177
	v_mov_b32_e32 v12, v177
	v_mov_b32_e32 v14, v177
	v_mov_b32_e32 v15, v177
	v_add_u32_e32 v206, 0x80, v169
	v_mov_b32_e32 v207, 0
	v_lshlrev_b64 v[206:207], 14, v[206:207]
	v_lshl_add_u64 v[206:207], v[174:175], 0, v[206:207]
	global_load_dwordx4 v[160:163], v[206:207], off nt

.Lrec_allin:
	s_cmp_lt_u32 s36, 23
	s_cbranch_scc0 .Lrec_nogx
	global_load_dwordx4 v[160:163], v[206:207], off nt
